# T3a: gamma_L moved to its own free LDS slot; the barrier between stage A and stage B removed (stage B only reads its own wave's stage A rows): stage I(n), A(n+1), B(n+1) run unsynchronised
# baseline (speedup 1.0000x reference)
; template <int CTRL> __device__ __forceinline__ float dpp16(float x) { return __builtin_bit_cast(float, __builtin_amdgcn_update_dpp(0, __builtin_bit_cast(int, x), CTRL, 0xf, 0xf, true)); }
; #define CK_BAR() do { asm volatile("s_waitcnt lgkmcnt(0)" ::: "memory"); __builtin_amdgcn_s_barrier(); asm volatile("" ::: "memory"); } while (0)
; __device__ __forceinline__ void phase1(const int WID_, const In& I, char* lds) {
;     ...
;             for (int e = 0; e < 8; ++e) { const int w_ = e >> 1; const bool hi = e & 1;
;                 auto ex = [&](unsigned u) { return hi ? __builtin_bit_cast(float, u & 0xffff0000u) : __builtin_bit_cast(float, u << 16); };
;                 float x = ex(wr[w_]); r_[e] = x + (ex(pr[w_]) - x) * mur[e];
;                 x = ex(wk[w_]); const float k = x + (ex(pk[w_]) - x) * muk[e];
;                 x = ex(wv4[w_]); v_[e] = x + (ex(pv[w_]) - x) * muv[e];
;                 a_[e] = ex(wa[w_]); kk_[e] = k * ckk[e]; ss += kk_[e] * kk_[e];
;                 kp_[e] = k * (1.f + (a_[e] - 1.f) * cka[e]); rk += r_[e] * kp_[e] * crk[e];
;                 G[s * 64 + cg * 8 + e] = ex(wl[w_]); }
;             ss += dpp16<0xB1>(ss); ss += dpp16<0x4E>(ss); ss += dpp16<0x141>(ss);
;             const float inv = 1.f / fmaxf(sqrtf(ss), 1e-12f);
; #pragma unroll
;             for (int e = 0; e < 8; ++e) { kk_[e] *= inv; b_[e] = kk_[e] * a_[e]; }
;     ...
;         CK_BAR();
;         { const int ch = tid & 63, part = tid >> 6; float run = 0.f;
; #pragma unroll
;           for (int i = 0; i < 8; ++i) { run += G[(8 * part + i) * 64 + ch]; G[(8 * part + i) * 64 + ch] = run; }
;           TOT[part * 64 + ch] = run; }
;         CK_BAR();
;         { const int ch = tid & 63, part = tid >> 6; float off = 0.f;
;           for (int p = 0; p < part; ++p) off += TOT[p * 64 + ch];
; #pragma unroll
;           for (int i = 0; i < 8; ++i) G[(8 * part + i) * 64 + ch] += off; }
.LBB0_1416:
	s_or_b64 exec, exec, s[6:7]
	v_and_b32_e32 v52, 63, v58
	v_ashrrev_i32_e32 v53, 6, v59
	v_lshlrev_b32_e32 v4, 11, v53
	v_lshlrev_b32_e32 v6, 2, v52
	s_waitcnt lgkmcnt(0)
	v_add3_u32 v4, s77, v4, v6
	ds_read2st64_b32 v[54:55], v4 offset1:1
	ds_read2st64_b32 v[174:175], v4 offset0:2 offset1:3
	ds_read2st64_b32 v[176:177], v4 offset0:4 offset1:5
	ds_read2st64_b32 v[178:179], v4 offset0:6 offset1:7
	v_mov_b32_e32 v5, 0
	v_cmp_lt_i32_e64 s[0:1], 0, v53
	s_waitcnt lgkmcnt(3)
	v_add_f32_e32 v7, 0, v54
	v_add_f32_e32 v63, v7, v55
	ds_write2st64_b32 v4, v7, v63 offset1:1
	s_waitcnt lgkmcnt(3)
	v_add_f32_e32 v7, v63, v174
	v_add_f32_e32 v63, v7, v175
	ds_write2st64_b32 v4, v7, v63 offset0:2 offset1:3
	s_waitcnt lgkmcnt(3)
	v_add_f32_e32 v7, v63, v176
	v_add_f32_e32 v63, v7, v177
	ds_write2st64_b32 v4, v7, v63 offset0:4 offset1:5
	s_waitcnt lgkmcnt(3)
	v_add_f32_e32 v7, v63, v178
	v_add_f32_e32 v54, v7, v179
	ds_write2st64_b32 v4, v7, v54 offset0:6 offset1:7
	v_lshl_add_u32 v7, v59, 2, 0
	v_add_u32_e32 v7, 0x21400, v7
	ds_write_b32 v7, v54
	s_waitcnt lgkmcnt(0)
	s_barrier
	v_readfirstlane_b32 s98, v53
	v_add_u32_e32 v6, 0x21400, v6
	ds_read_b32 v174, v6
	ds_read_b32 v175, v6 offset:256
	ds_read_b32 v176, v6 offset:512
	ds_read_b32 v177, v6 offset:768
	ds_read_b32 v178, v6 offset:1024
	ds_read_b32 v179, v6 offset:1280
	ds_read_b32 v180, v6 offset:1536
	s_cmp_lt_u32 s98, 1
	s_cbranch_scc1 .Lscan_done
	s_waitcnt lgkmcnt(6)
	v_add_f32_e32 v5, v5, v174
	s_cmp_lt_u32 s98, 2
	s_cbranch_scc1 .Lscan_done
	s_waitcnt lgkmcnt(5)
	v_add_f32_e32 v5, v5, v175
	s_cmp_lt_u32 s98, 3
	s_cbranch_scc1 .Lscan_done
	s_waitcnt lgkmcnt(4)
	v_add_f32_e32 v5, v5, v176
	s_cmp_lt_u32 s98, 4
	s_cbranch_scc1 .Lscan_done
	s_waitcnt lgkmcnt(3)
	v_add_f32_e32 v5, v5, v177
	s_cmp_lt_u32 s98, 5
	s_cbranch_scc1 .Lscan_done
	s_waitcnt lgkmcnt(2)
	v_add_f32_e32 v5, v5, v178
	s_cmp_lt_u32 s98, 6
	s_cbranch_scc1 .Lscan_done
	s_waitcnt lgkmcnt(1)
	v_add_f32_e32 v5, v5, v179
	s_cmp_lt_u32 s98, 7
	s_cbranch_scc1 .Lscan_done
	s_waitcnt lgkmcnt(0)
	v_add_f32_e32 v5, v5, v180
.Lscan_done:
	s_waitcnt lgkmcnt(0)
	v_cndmask_b32_e32 v6, 0, v24, vcc
	v_cndmask_b32_e32 v7, 0, v26, vcc
	v_cndmask_b32_e32 v24, 0, v25, vcc
	v_cndmask_b32_e32 v25, 0, v27, vcc
	v_lshlrev_b32_e32 v26, 16, v20
	v_lshlrev_b32_e32 v27, 16, v6
	v_and_b32_e32 v20, 0xffff0000, v20
	v_and_b32_e32 v6, 0xffff0000, v6
	v_sub_f32_e32 v27, v27, v26
	v_sub_f32_e32 v6, v6, v20
	v_fma_mix_f32 v53, v27, v0, v26 op_sel_hi:[0,1,0]
	v_fma_mix_f32 v68, v6, v0, v20 op_sel:[0,1,0] op_sel_hi:[0,1,0]
	v_lshlrev_b32_e32 v0, 16, v21
	v_lshlrev_b32_e32 v6, 16, v24
	v_sub_f32_e32 v6, v6, v0
	v_fma_mix_f32 v72, v6, v1, v0 op_sel_hi:[0,1,0]
	v_and_b32_e32 v0, 0xffff0000, v21
	v_and_b32_e32 v6, 0xffff0000, v24
	v_sub_f32_e32 v6, v6, v0
	v_fma_mix_f32 v73, v6, v1, v0 op_sel:[0,1,0] op_sel_hi:[0,1,0]
	v_lshlrev_b32_e32 v0, 16, v22
	v_lshlrev_b32_e32 v1, 16, v7
	v_sub_f32_e32 v1, v1, v0
	v_fma_mix_f32 v74, v1, v2, v0 op_sel_hi:[0,1,0]
	v_and_b32_e32 v0, 0xffff0000, v22
	v_and_b32_e32 v1, 0xffff0000, v7
	v_sub_f32_e32 v1, v1, v0
	v_fma_mix_f32 v75, v1, v2, v0 op_sel:[0,1,0] op_sel_hi:[0,1,0]
	v_add_f32_e32 v2, v56, v57
	s_mov_b32 s0, 0xf800000
	v_mul_f32_e32 v6, 0x4f800000, v2
	v_cmp_gt_f32_e32 vcc, s0, v2
	v_lshlrev_b32_e32 v0, 16, v23
	v_lshlrev_b32_e32 v1, 16, v25
	v_cndmask_b32_e32 v2, v2, v6, vcc
	v_sqrt_f32_e32 v6, v2
	v_sub_f32_e32 v1, v1, v0
	v_fma_mix_f32 v78, v1, v3, v0 op_sel_hi:[0,1,0]
	v_and_b32_e32 v0, 0xffff0000, v23
	v_add_u32_e32 v1, -1, v6
	v_fma_f32 v7, -v1, v6, v2
	v_cmp_ge_f32_e64 s[0:1], 0, v7
	v_add_u32_e32 v7, 1, v6
	v_lshlrev_b32_e32 v52, 3, v61
	v_cndmask_b32_e64 v1, v6, v1, s[0:1]
	v_fma_f32 v6, -v7, v6, v2
	v_cmp_lt_f32_e64 s[0:1], 0, v6
	s_add_i32 s33, s40, s94
	s_nop 0
	v_cndmask_b32_e64 v1, v1, v7, s[0:1]
	v_mul_f32_e32 v6, 0x37800000, v1
	v_cndmask_b32_e32 v1, v1, v6, vcc
	v_cmp_class_f32_e32 vcc, v2, v77
	v_and_b32_e32 v7, 0xffff0000, v25
	v_sub_f32_e32 v7, v7, v0
	v_cndmask_b32_e32 v1, v1, v2, vcc
	v_max_f32_e32 v1, 0x2b8cbccc, v1
	v_div_scale_f32 v2, s[0:1], v1, v1, 1.0
	v_rcp_f32_e32 v6, v2
	v_fma_mix_f32 v79, v7, v3, v0 op_sel:[0,1,0] op_sel_hi:[0,1,0]
	s_movk_i32 s0, 0xff00
	s_min_i32 s1, s33, 0x1fff
	v_fma_f32 v0, -v2, v6, 1.0
	v_fmac_f32_e32 v6, v0, v6
	v_div_scale_f32 v0, vcc, 1.0, v1, 1.0
	v_mul_f32_e32 v3, v0, v6
	v_fma_f32 v7, -v2, v3, v0
	v_fmac_f32_e32 v3, v7, v6
	v_fma_f32 v0, -v2, v3, v0
	v_div_fmas_f32 v0, v0, v6, v3
	v_div_fixup_f32 v0, v0, v1, 1.0
	v_pk_mul_f32 v[54:55], v[8:9], v[0:1] op_sel_hi:[1,0]
	v_pk_mul_f32 v[50:51], v[50:51], v[0:1] op_sel_hi:[1,0]
	v_pk_mul_f32 v[66:67], v[10:11], v[0:1] op_sel_hi:[1,0]
	v_pk_mul_f32 v[48:49], v[48:49], v[0:1] op_sel_hi:[1,0]
	ds_read2st64_b32 v[0:1], v4 offset1:1
	ds_read2st64_b32 v[2:3], v4 offset0:2 offset1:3
	ds_read2st64_b32 v[6:7], v4 offset0:4 offset1:5
	ds_read2st64_b32 v[8:9], v4 offset0:6 offset1:7
	v_pk_mul_f32 v[56:57], v[54:55], v[44:45]
	v_pk_mul_f32 v[64:65], v[50:51], v[42:43]
	v_cmp_lt_i32_e32 vcc, 0, v60
	s_waitcnt lgkmcnt(3)
	v_add_f32_e32 v0, v5, v0
	v_add_f32_e32 v1, v5, v1
	ds_write2st64_b32 v4, v0, v1 offset1:1
	s_waitcnt lgkmcnt(3)
	v_add_f32_e32 v0, v5, v2
	v_add_f32_e32 v1, v5, v3
	ds_write2st64_b32 v4, v0, v1 offset0:2 offset1:3
	s_waitcnt lgkmcnt(3)
	v_add_f32_e32 v0, v5, v6
	v_add_f32_e32 v1, v5, v7
	ds_write2st64_b32 v4, v0, v1 offset0:4 offset1:5
	s_waitcnt lgkmcnt(3)
	v_add_f32_e32 v0, v5, v8
	v_add_f32_e32 v1, v5, v9
	ds_write2st64_b32 v4, v0, v1 offset0:6 offset1:7
	v_max_i32_e32 v0, 1, v60
	v_lshl_add_u32 v0, v0, 8, s77
	v_lshlrev_b32_e32 v1, 2, v52
	s_waitcnt lgkmcnt(0)
	s_barrier
; __device__ __forceinline__ unsigned pk2(float lo, float hi) { const f32x2h v = {lo, hi}; const bf16x2h b = __builtin_convertvector(v, bf16x2h); return __builtin_bit_cast(unsigned, b); }
; __device__ __forceinline__ void phase1(const int WID_, const In& I, char* lds) {
;     ...
;             const float4 g0_ = *(const float4*)(G + s * 64 + cg * 8), g1_ = *(const float4*)(G + s * 64 + cg * 8 + 4);
;             const int sm = (s > 0) ? s - 1 : 0; const float msk = (s > 0) ? 1.f : 0.f;
;             const float4 m0_ = *(const float4*)(G + sm * 64 + cg * 8), m1_ = *(const float4*)(G + sm * 64 + cg * 8 + 4);
;             const float4 l0_ = *(const float4*)(G + 63 * 64 + cg * 8), l1_ = *(const float4*)(G + 63 * 64 + cg * 8 + 4);
;             const float gv_[8] = {g0_.x, g0_.y, g0_.z, g0_.w, g1_.x, g1_.y, g1_.z, g1_.w}, mv_[8] = {m0_.x, m0_.y, m0_.z, m0_.w, m1_.x, m1_.y, m1_.z, m1_.w}, lv_[8] = {l0_.x, l0_.y, l0_.z, l0_.w, l1_.x, l1_.y, l1_.z, l1_.w};
; #pragma unroll
;             for (int e = 0; e < 8; ++e) { const float g = gv_[e], gm1 = mv_[e] * msk, gL = lv_[e];
;                 glast[e] = gL;
;                 const float eg = __expf(g), eng = __expf(-g), egm = __expf(gm1), egl = __expf(gL - g);
;                 ab[e] = -kk_[e] * egm; rb[e] = r_[e] * eg; bb[e] = b_[e] * eng; kb[e] = kp_[e] * eng; bt[e] = b_[e] * egl; kt[e] = kp_[e] * egl; }
; #pragma unroll
;             for (int q = 0; q < 4; ++q) { pab[q] = pk2(ab[2 * q], ab[2 * q + 1]); prb[q] = pk2(rb[2 * q], rb[2 * q + 1]); pbb[q] = pk2(bb[2 * q], bb[2 * q + 1]); pkb[q] = pk2(kb[2 * q], kb[2 * q + 1]); }
;             *(uint4*)(MAT(O_AB) + s * LD + cg * 8) = make_uint4(pab[0], pab[1], pab[2], pab[3]);
;             *(uint4*)(MAT(O_RB) + s * LD + cg * 8) = make_uint4(prb[0], prb[1], prb[2], prb[3]);
;             *(uint4*)(MAT(O_BB) + s * LD + cg * 8) = make_uint4(pbb[0], pbb[1], pbb[2], pbb[3]);
;             *(uint4*)(MAT(O_KB) + s * LD + cg * 8) = make_uint4(pkb[0], pkb[1], pkb[2], pkb[3]);
	v_add3_u32 v0, v0, v1, s0
	ds_read_b128 v[8:11], v62
	ds_read_b128 v[20:23], v62 offset:16
	ds_read_b128 v[24:27], v0
	ds_read_b128 v[42:45], v0 offset:16
	v_add_u32_e32 v0, 0, v1
	v_add_u32_e32 v0, 0x21300, v0
	ds_read_b128 v[4:7], v0
	ds_read_b128 v[0:3], v0 offset:16
	v_cndmask_b32_e64 v80, 0, 1.0, vcc
	s_waitcnt lgkmcnt(3)
	v_mul_f32_e32 v63, v80, v24
	v_mul_f32_e32 v24, 0x3fb8aa3b, v8
	v_mul_f32_e32 v62, 0xbfb8aa3b, v8
	s_waitcnt lgkmcnt(1)
	v_sub_f32_e32 v8, v4, v8
	v_mul_f32_e32 v8, 0x3fb8aa3b, v8
	v_exp_f32_e32 v8, v8
	v_mul_f32_e32 v63, 0x3fb8aa3b, v63
	v_exp_f32_e32 v70, v63
	v_mul_f32_e32 v63, 0xbfb8aa3b, v9
	v_mul_f32_e32 v81, v56, v8
	v_mul_f32_e32 v82, v14, v8
	v_mul_f32_e32 v8, v80, v25
	v_mul_f32_e32 v8, 0x3fb8aa3b, v8
	v_exp_f32_e32 v71, v8
	v_sub_f32_e32 v8, v5, v9
	v_mul_f32_e32 v25, 0x3fb8aa3b, v9
	v_mul_f32_e32 v8, 0x3fb8aa3b, v8
	v_exp_f32_e32 v24, v24
	v_exp_f32_e32 v62, v62
	v_exp_f32_e32 v25, v25
	v_exp_f32_e32 v63, v63
	v_exp_f32_e32 v8, v8
	v_mul_f32_e32 v9, v80, v26
	v_pk_mul_f32 v[12:13], v[12:13], v[24:25]
	v_pk_mul_f32 v[24:25], v[56:57], v[62:63]
	v_pk_mul_f32 v[62:63], v[14:15], v[62:63]
	v_mul_f32_e32 v56, v57, v8
	v_mul_f32_e32 v57, v15, v8
	v_mul_f32_e32 v8, 0x3fb8aa3b, v10
	v_mul_f32_e32 v14, 0xbfb8aa3b, v10
	v_sub_f32_e32 v10, v6, v10
	v_mul_f32_e32 v10, 0x3fb8aa3b, v10
	v_exp_f32_e32 v10, v10
	v_pk_mul_f32 v[54:55], v[70:71], v[54:55] neg_lo:[0,1] neg_hi:[0,1]
	v_mul_f32_e32 v9, 0x3fb8aa3b, v9
	v_exp_f32_e32 v26, v9
	v_mul_f32_e32 v70, v64, v10
	v_mul_f32_e32 v71, v28, v10
	v_mul_f32_e32 v10, v80, v27
	v_mul_f32_e32 v9, 0x3fb8aa3b, v11
	v_mul_f32_e32 v15, 0xbfb8aa3b, v11
	v_mul_f32_e32 v10, 0x3fb8aa3b, v10
	v_exp_f32_e32 v8, v8
	v_exp_f32_e32 v14, v14
	v_exp_f32_e32 v9, v9
	v_exp_f32_e32 v15, v15
	v_exp_f32_e32 v27, v10
	v_sub_f32_e32 v10, v7, v11
	v_mul_f32_e32 v10, 0x3fb8aa3b, v10
	v_exp_f32_e32 v83, v10
	v_pk_mul_f32 v[50:51], v[26:27], v[50:51] neg_lo:[0,1] neg_hi:[0,1]
	v_pk_mul_f32 v[10:11], v[36:37], v[8:9]
	v_pk_mul_f32 v[26:27], v[64:65], v[14:15]
	v_pk_mul_f32 v[14:15], v[28:29], v[14:15]
	v_mul_f32_e32 v8, 0x3fb8aa3b, v20
	v_mul_f32_e32 v28, 0xbfb8aa3b, v20
	s_waitcnt lgkmcnt(0)
	v_sub_f32_e32 v20, v0, v20
	v_mul_f32_e32 v20, 0x3fb8aa3b, v20
	v_exp_f32_e32 v20, v20
	v_pk_mul_f32 v[46:47], v[66:67], v[46:47]
	v_mul_f32_e32 v64, v65, v83
	v_mul_f32_e32 v65, v29, v83
	v_mul_f32_e32 v83, v46, v20
	v_mul_f32_e32 v84, v40, v20
	v_mul_f32_e32 v20, v80, v43
	v_mul_f32_e32 v9, v80, v42
	v_mul_f32_e32 v20, 0x3fb8aa3b, v20
	v_mul_f32_e32 v9, 0x3fb8aa3b, v9
	v_exp_f32_e32 v37, v20
	v_sub_f32_e32 v20, v1, v21
	v_exp_f32_e32 v36, v9
	v_mul_f32_e32 v9, 0x3fb8aa3b, v21
	v_mul_f32_e32 v29, 0xbfb8aa3b, v21
	v_mul_f32_e32 v20, 0x3fb8aa3b, v20
	v_sub_f32_e32 v21, v2, v22
	v_exp_f32_e32 v8, v8
	v_exp_f32_e32 v9, v9
	v_exp_f32_e32 v20, v20
	v_mul_f32_e32 v21, 0x3fb8aa3b, v21
	v_exp_f32_e32 v21, v21
	v_exp_f32_e32 v28, v28
	v_exp_f32_e32 v29, v29
	v_pk_mul_f32 v[34:35], v[48:49], v[34:35]
	v_pk_mul_f32 v[36:37], v[36:37], v[66:67] neg_lo:[0,1] neg_hi:[0,1]
	v_pk_mul_f32 v[32:33], v[32:33], v[8:9]
	v_mul_f32_e32 v66, v47, v20
	v_mul_f32_e32 v67, v41, v20
	v_mul_f32_e32 v9, v80, v44
	v_mul_f32_e32 v8, 0x3fb8aa3b, v22
	v_mul_f32_e32 v20, 0xbfb8aa3b, v22
	v_mul_f32_e32 v22, v80, v45
	v_mul_f32_e32 v9, 0x3fb8aa3b, v9
	v_mul_f32_e32 v85, v34, v21
	v_mul_f32_e32 v86, v30, v21
	v_mul_f32_e32 v21, 0xbfb8aa3b, v23
	v_mul_f32_e32 v22, 0x3fb8aa3b, v22
	v_pk_mul_f32 v[42:43], v[46:47], v[28:29]
	v_pk_mul_f32 v[28:29], v[40:41], v[28:29]
	v_exp_f32_e32 v20, v20
	v_exp_f32_e32 v40, v9
	v_mul_f32_e32 v9, 0x3fb8aa3b, v23
	v_exp_f32_e32 v21, v21
	v_exp_f32_e32 v41, v22
	v_sub_f32_e32 v22, v3, v23
	v_exp_f32_e32 v8, v8
	v_exp_f32_e32 v9, v9
	v_mul_f32_e32 v22, 0x3fb8aa3b, v22
	v_exp_f32_e32 v22, v22
	v_pk_mul_f32 v[40:41], v[40:41], v[48:49] neg_lo:[0,1] neg_hi:[0,1]
	v_pk_mul_f32 v[44:45], v[34:35], v[20:21]
	v_pk_mul_f32 v[46:47], v[30:31], v[20:21]
	v_cvt_pk_bf16_f32 v21, v26, v27
	v_cvt_pk_bf16_f32 v26, v28, v29
	v_mul_lo_u32 v28, v60, s9
	v_lshlrev_b32_e32 v29, 1, v52
	v_pk_mul_f32 v[38:39], v[38:39], v[8:9]
	v_cvt_pk_bf16_f32 v8, v54, v55
	v_cvt_pk_bf16_f32 v12, v12, v13
	v_cvt_pk_bf16_f32 v9, v50, v51
	v_cvt_pk_bf16_f32 v13, v10, v11
	v_cvt_pk_bf16_f32 v10, v36, v37
	v_cvt_pk_bf16_f32 v11, v40, v41
	v_add3_u32 v28, 0, v28, v29
	v_mul_f32_e32 v30, v35, v22
	v_mul_f32_e32 v31, v31, v22
	v_cvt_pk_bf16_f32 v20, v24, v25
	v_cvt_pk_bf16_f32 v24, v62, v63
	v_cvt_pk_bf16_f32 v25, v14, v15
	v_cvt_pk_bf16_f32 v14, v32, v33
	v_cvt_pk_bf16_f32 v22, v42, v43
	v_cvt_pk_bf16_f32 v15, v38, v39
	v_cvt_pk_bf16_f32 v23, v44, v45
	v_cvt_pk_bf16_f32 v27, v46, v47
	ds_write_b128 v28, v[8:11]
	ds_write_b128 v28, v[12:15] offset:9216
	ds_write_b128 v28, v[20:23] offset:18432
	ds_write_b128 v28, v[24:27] offset:27648
	v_and_b32_e32 v35, 2, v61
	v_cmp_ne_u32_e64 s[98:99], 0, v35
	v_bfe_i32 v35, v61, 0, 1
	v_bfe_i32 v38, v60, 0, 1
	v_and_b32_e32 v35, 0x2020202, v35
	v_and_b32_e32 v38, 0x6060606, v38
	v_xor_b32_e32 v32, 0x5040100, v35
	v_xor_b32_e32 v32, v32, v38
	v_and_b32_e32 v33, 3, v61
	v_xor_b32_e32 v33, v60, v33
	v_and_b32_e32 v33, 7, v33
	v_lshl_add_u32 v33, v61, 3, v33
	v_mul_u32_u24_e32 v33, 0x90, v33
	v_and_b32_e32 v34, -8, v60
	v_lshl_add_u32 v33, v34, 1, v33
	v_add_u32_e32 v34, 0x12000, v33
	v_cvt_pk_bf16_f32 v81, v81, v56
	v_cvt_pk_bf16_f32 v70, v70, v64
; __device__ __forceinline__ bf16 f2bf(float f) { return (bf16)(pk2(f, f) & 0xffffu); }
; #define CK_BAR() do { asm volatile("s_waitcnt lgkmcnt(0)" ::: "memory"); __builtin_amdgcn_s_barrier(); asm volatile("" ::: "memory"); } while (0)
; __device__ __forceinline__ void phase1(const int WID_, const In& I, char* lds) {
;     ...
;             for (int e = 0; e < 8; ++e) { const int k = cg * 8 + e;
;                 MAT(O_AT)[k * LD + s] = f2bf(ab[e]); MAT(O_BT)[k * LD + s] = f2bf(bt[e]); MAT(O_KT)[k * LD + s] = f2bf(kt[e]); MAT(O_VT)[k * LD + s] = f2bf(v_[e]); }
;         }
;         CK_BAR();
;         P1_LOADS(item + GN);
;         if (s == 63) {
; #pragma unroll
;             for (int e = 0; e < 8; ++e) TOT[cg * 8 + e] = __expf(glast[e]);
	v_cvt_pk_bf16_f32 v83, v83, v66
	v_cvt_pk_bf16_f32 v85, v85, v30
	v_cvt_pk_bf16_f32 v82, v82, v57
	v_cvt_pk_bf16_f32 v71, v71, v65
	v_cvt_pk_bf16_f32 v84, v84, v67
	v_cvt_pk_bf16_f32 v86, v86, v31
	v_cvt_pk_bf16_f32 v53, v53, v68
	v_cvt_pk_bf16_f32 v72, v72, v73
	v_cvt_pk_bf16_f32 v74, v74, v75
	v_cvt_pk_bf16_f32 v78, v78, v79
	v_mov_b32_dpp v55, v8 row_ror:8 row_mask:0xf bank_mask:0xf
	v_mov_b32_dpp v51, v9 row_ror:8 row_mask:0xf bank_mask:0xf
	v_mov_b32_dpp v37, v10 row_ror:8 row_mask:0xf bank_mask:0xf
	v_mov_b32_dpp v41, v11 row_ror:8 row_mask:0xf bank_mask:0xf
	v_mov_b32_dpp v56, v81 row_ror:8 row_mask:0xf bank_mask:0xf
	v_mov_b32_dpp v64, v70 row_ror:8 row_mask:0xf bank_mask:0xf
	v_mov_b32_dpp v66, v83 row_ror:8 row_mask:0xf bank_mask:0xf
	v_mov_b32_dpp v30, v85 row_ror:8 row_mask:0xf bank_mask:0xf
	v_mov_b32_dpp v57, v82 row_ror:8 row_mask:0xf bank_mask:0xf
	v_mov_b32_dpp v65, v71 row_ror:8 row_mask:0xf bank_mask:0xf
	v_mov_b32_dpp v67, v84 row_ror:8 row_mask:0xf bank_mask:0xf
	v_mov_b32_dpp v31, v86 row_ror:8 row_mask:0xf bank_mask:0xf
	v_mov_b32_dpp v68, v53 row_ror:8 row_mask:0xf bank_mask:0xf
	v_mov_b32_dpp v73, v72 row_ror:8 row_mask:0xf bank_mask:0xf
	v_mov_b32_dpp v75, v74 row_ror:8 row_mask:0xf bank_mask:0xf
	v_mov_b32_dpp v79, v78 row_ror:8 row_mask:0xf bank_mask:0xf
	v_perm_b32 v54, v55, v8, v32
	v_perm_b32 v50, v51, v9, v32
	v_perm_b32 v36, v37, v10, v32
	v_perm_b32 v40, v41, v11, v32
	v_perm_b32 v81, v56, v81, v32
	v_perm_b32 v70, v64, v70, v32
	v_perm_b32 v83, v66, v83, v32
	v_perm_b32 v85, v30, v85, v32
	v_perm_b32 v82, v57, v82, v32
	v_perm_b32 v71, v65, v71, v32
	v_perm_b32 v84, v67, v84, v32
	v_perm_b32 v86, v31, v86, v32
	v_perm_b32 v53, v68, v53, v32
	v_perm_b32 v72, v73, v72, v32
	v_perm_b32 v74, v75, v74, v32
	v_perm_b32 v78, v79, v78, v32
	v_cndmask_b32_e64 v8, v54, v50, s[98:99]
	v_cndmask_b32_e64 v9, v50, v54, s[98:99]
	v_cndmask_b32_e64 v10, v36, v40, s[98:99]
	v_cndmask_b32_e64 v11, v40, v36, s[98:99]
	v_cndmask_b32_e64 v12, v81, v70, s[98:99]
	v_cndmask_b32_e64 v13, v70, v81, s[98:99]
	v_cndmask_b32_e64 v14, v83, v85, s[98:99]
	v_cndmask_b32_e64 v15, v85, v83, s[98:99]
	v_cndmask_b32_e64 v20, v82, v71, s[98:99]
	v_cndmask_b32_e64 v21, v71, v82, s[98:99]
	v_cndmask_b32_e64 v22, v84, v86, s[98:99]
	v_cndmask_b32_e64 v23, v86, v84, s[98:99]
	v_cndmask_b32_e64 v24, v53, v72, s[98:99]
	v_cndmask_b32_e64 v25, v72, v53, s[98:99]
	v_cndmask_b32_e64 v26, v74, v78, s[98:99]
	v_cndmask_b32_e64 v27, v78, v74, s[98:99]
	v_permlane16_swap_b32_e32 v8, v9
	v_permlane16_swap_b32_e32 v10, v11
	v_permlane16_swap_b32_e32 v12, v13
	v_permlane16_swap_b32_e32 v14, v15
	v_permlane16_swap_b32_e32 v20, v21
	v_permlane16_swap_b32_e32 v22, v23
	v_permlane16_swap_b32_e32 v24, v25
	v_permlane16_swap_b32_e32 v26, v27
	v_permlane32_swap_b32_e32 v8, v10
	v_permlane32_swap_b32_e32 v9, v11
	v_permlane32_swap_b32_e32 v12, v14
	v_permlane32_swap_b32_e32 v13, v15
	v_permlane32_swap_b32_e32 v20, v22
	v_permlane32_swap_b32_e32 v21, v23
	v_permlane32_swap_b32_e32 v24, v26
	v_permlane32_swap_b32_e32 v25, v27
	s_nop 1
	ds_write_b128 v33, v[8:11] offset:36864
	ds_write_b128 v33, v[12:15] offset:55296
	ds_write_b128 v33, v[20:23] offset:64512
	ds_write_b128 v34, v[24:27]
	s_waitcnt lgkmcnt(0)
	s_barrier
	v_mbcnt_lo_u32_b32 v8, -1, 0
	v_mbcnt_hi_u32_b32 v8, -1, v8
	s_ashr_i32 s0, s1, 10
	v_add_u32_e32 v9, s86, v8
	s_lshr_b32 s4, s1, 1
	s_lshl_b32 s1, s1, 6
	v_ashrrev_i32_e32 v9, 3, v9
	s_and_b32 s4, s4, 0x1c0
	v_lshlrev_b32_e32 v8, 3, v8
	s_and_b32 s1, s1, 0x1fc0
	v_and_or_b32 v14, v8, 56, s4
	v_add_u32_e32 v8, s1, v9
	s_ashr_i32 s1, s0, 31
	s_lshl_b64 s[0:1], s[0:1], 13
	v_ashrrev_i32_e32 v9, 31, v8
	v_lshl_add_u64 v[10:11], s[0:1], 0, v[8:9]
	v_mov_b64_e32 v[12:13], s[92:93]
	v_mad_u64_u32 v[12:13], s[0:1], v10, s8, v[12:13]
	v_mad_i32_i24 v13, v11, s8, v13
	v_lshlrev_b32_e32 v68, 1, v14
	v_cmp_lt_i32_e32 vcc, 0, v8
	v_lshl_add_u64 v[12:13], v[12:13], 0, v[68:69]
	v_readlane_b32 s0, v242, 37
	v_cndmask_b32_e64 v9, 0, -1, vcc
	v_cndmask_b32_e32 v8, 0, v76, vcc
	v_lshl_add_u64 v[8:9], v[12:13], 0, v[8:9]
	global_load_dwordx4 v[36:39], v[12:13], off
	global_load_dwordx4 v[28:31], v[12:13], off offset:1024
	global_load_dwordx4 v[20:23], v[12:13], off offset:2048
	global_load_dwordx4 v[44:47], v[8:9], off
	global_load_dwordx4 v[48:51], v[8:9], off offset:1024
	global_load_dwordx4 v[24:27], v[8:9], off offset:2048
	v_lshlrev_b64 v[8:9], 10, v[10:11]
	v_readlane_b32 s1, v242, 38
	v_cmp_eq_u32_e32 vcc, 63, v60
	s_nop 0
	v_lshl_add_u64 v[10:11], s[0:1], 0, v[8:9]
	v_lshl_add_u64 v[10:11], v[10:11], 0, v[68:69]
	v_lshl_add_u64 v[8:9], s[28:29], 0, v[8:9]
	v_lshl_add_u64 v[8:9], v[8:9], 0, v[68:69]
	global_load_dwordx4 v[32:35], v[10:11], off
	global_load_dwordx4 v[40:43], v[8:9], off
	s_and_saveexec_b64 s[0:1], vcc
	s_cbranch_execz .LBB0_1428
	v_mul_f32_e32 v4, 0x3fb8aa3b, v4
	v_mul_f32_e32 v5, 0x3fb8aa3b, v5
	v_mul_f32_e32 v6, 0x3fb8aa3b, v6
	v_mul_f32_e32 v7, 0x3fb8aa3b, v7
	v_exp_f32_e32 v4, v4
	v_exp_f32_e32 v5, v5
	v_exp_f32_e32 v6, v6
	v_exp_f32_e32 v7, v7
	v_mul_f32_e32 v0, 0x3fb8aa3b, v0
	v_mul_f32_e32 v1, 0x3fb8aa3b, v1
	v_mul_f32_e32 v2, 0x3fb8aa3b, v2
	v_mul_f32_e32 v3, 0x3fb8aa3b, v3
	v_exp_f32_e32 v0, v0
	v_exp_f32_e32 v1, v1
	v_exp_f32_e32 v2, v2
	v_exp_f32_e32 v3, v3
	v_lshl_add_u32 v8, v52, 2, 0
	v_add_u32_e32 v8, 0x23400, v8
	ds_write_b128 v8, v[4:7]
	ds_write_b128 v8, v[0:3] offset:16

; __device__ __forceinline__ void phase1(const int WID_, const In& I, char* lds) {
;     ...
;         { const int st = wv >> 2, ct = wv & 3;
;           f32x16 acc = mm_tile<64>(zero16(), MAT(O_TM) + 32 * st * LD, LD, MAT(O_AT) + 32 * ct * LD, LD, lane);
;           CK_BAR();
;           store_tr(acc, MAT(O_X1T) + 32 * ct * LD + 32 * st, LD, lane); }
;         CK_BAR();
; #pragma unroll
;         for (int ti = 0; ti < 2; ++ti) {
;             const int u = wv + 8 * ti;
;             const int kind = u >> 2, t0 = (u >> 1) & 1, t1 = u & 1, hh = lane >> 5, cc = lane & 31;
;             uint2 w[4]; bf16* dbase;
;             if (kind < 2) {
;                 f32x16 acc = mm_tile<64>(zero16(), MAT(kind == 0 ? O_BT : O_ARB) + 32 * t0 * LD, LD, MAT(O_X1T) + (64 + 32 * t1) * LD, LD, lane);
;                 acc = mm_tile<64>(acc, MAT(kind == 0 ? O_KT : O_ARK) + 32 * t0 * LD, LD, MAT(O_VT) + 32 * t1 * LD, LD, lane);
;                 const int col = 32 * t1 + cc;
;                 dbase = (bf16*)(out + (kind == 0 ? 16384 : 24576)) + ((2 * t0 * 4 + (col >> 4)) * 64 + (col & 15) + 16 * hh) * 4;
; #pragma unroll
;                 for (int g = 0; g < 4; ++g) { w[g].x = cvtpk(acc[4 * g], acc[4 * g + 1]); w[g].y = cvtpk(acc[4 * g + 2], acc[4 * g + 3]); }
;             } else if (kind == 2) {
;                 f32x16 acc = mm_tile<64>(zero16(), MAT(O_X1T) + 32 * t0 * LD, LD, MAT(O_BT) + 32 * t1 * LD, LD, lane);
;                 const int k = 32 * t1 + cc; const float gl = TOT[k];
;                 dbase = (bf16*)out + k * 64 + 32 * t0 + 4 * hh;
; #pragma unroll
;                 for (int g = 0; g < 4; ++g) { float x[4];
; #pragma unroll
;                     for (int e = 0; e < 4; ++e) { const int kp = 32 * t0 + 8 * g + 4 * hh + e; x[e] = acc[4 * g + e] + ((kp == k) ? gl : 0.f); }
;                     w[g].x = cvtpk(x[0], x[1]); w[g].y = cvtpk(x[2], x[3]); }
;             } else {
;                 f32x16 acc = mm_tile<64>(zero16(), MAT(O_X1T) + 32 * t0 * LD, LD, MAT(O_ARB) + 32 * t1 * LD, LD, lane);
;                 const int sq = 32 * t1 + cc;
;                 dbase = (bf16*)(out + 8192) + sq * 64 + 32 * t0 + 4 * hh;
;                 const bf16* rb = MAT(O_RB) + sq * LD + 32 * t0;
; #pragma unroll
;                 for (int g = 0; g < 4; ++g) { const uint2 rr = *(const uint2*)(rb + 8 * g + 4 * hh);
.LBB0_1460:
	v_lshlrev_b32_e32 v86, 1, v53
	v_lshlrev_b32_e32 v87, 1, v0
	s_waitcnt lgkmcnt(0)
	s_barrier
	v_add3_u32 v53, s53, v86, v87
	ds_read_b128 v[0:3], v53
	v_add3_u32 v68, s58, v86, v87
	ds_read_b128 v[4:7], v68 offset:36864
	ds_read_b128 v[54:57], v53 offset:32
	ds_read_b128 v[60:63], v68 offset:36896
	ds_read_b128 v[64:67], v53 offset:64
	v_lshlrev_b32_e32 v58, 1, v58
	s_waitcnt lgkmcnt(3)
	v_mfma_f32_32x32x16_bf16 v[0:15], v[0:3], v[4:7], 0
	s_ashr_i32 s41, s40, 31
	s_lshl_b64 s[0:1], s[40:41], 15
	v_or_b32_e32 v81, s62, v78
	s_add_u32 s0, s90, s0
	s_addc_u32 s1, s91, s1
	s_add_i32 s4, 0, 0x18c00
	v_add3_u32 v85, s4, v86, v87
	s_waitcnt lgkmcnt(1)
	v_mfma_f32_32x32x16_bf16 v[0:15], v[54:57], v[60:63], v[0:15]
	ds_read_b128 v[54:57], v68 offset:36928
	v_add3_u32 v62, s59, v86, v58
	ds_read_b128 v[58:61], v53 offset:96
	ds_read_b128 v[70:73], v68 offset:36960
	v_add_u32_e32 v53, 0x4800, v62
	v_lshlrev_b32_e32 v68, 7, v81
	s_waitcnt lgkmcnt(2)
	v_mfma_f32_32x32x16_bf16 v[0:15], v[64:67], v[54:57], v[0:15]
	s_lshl_b32 s4, s60, 1
	v_add3_u32 v82, 0, v86, v87
	s_mov_b64 s[6:7], 0x2000
	s_and_b64 vcc, exec, s[20:21]
	v_add_u32_e32 v88, s61, v82
	s_waitcnt lgkmcnt(0)
	v_mfma_f32_32x32x16_bf16 v[0:15], v[58:61], v[70:73], v[0:15]
	s_nop 11
	v_cvt_pk_bf16_f32 v0, v0, v1
	v_cvt_pk_bf16_f32 v1, v2, v3
	v_cvt_pk_bf16_f32 v2, v4, v5
	v_cvt_pk_bf16_f32 v3, v6, v7
	v_cvt_pk_bf16_f32 v4, v8, v9
	v_cvt_pk_bf16_f32 v5, v10, v11
	v_cvt_pk_bf16_f32 v6, v12, v13
	v_cvt_pk_bf16_f32 v7, v14, v15
	ds_write2_b64 v53, v[0:1], v[2:3] offset1:2
	ds_write2_b64 v53, v[4:5], v[6:7] offset0:4 offset1:6
	v_lshl_add_u64 v[0:1], s[0:1], 0, v[68:69]
	s_waitcnt lgkmcnt(0)
	s_barrier
	v_ashrrev_i32_e32 v53, 31, v52
	v_lshl_add_u64 v[0:1], v[0:1], 0, s[4:5]
	v_lshl_add_u64 v[70:71], v[52:53], 1, v[0:1]
	v_mul_u32_u24_e32 v0, 0x90, v81
	v_lshlrev_b32_e32 v1, 3, v79
	s_add_i32 s4, 0, 0x23400
	v_lshl_add_u64 v[72:73], v[70:71], 0, s[6:7]
	v_add3_u32 v84, s66, v0, v1
	v_lshl_add_u32 v83, v81, 2, s4
	v_add_u32_e32 v68, s60, v52
	s_mov_b64 s[6:7], -1
	s_cbranch_vccz .LBB0_1466
	ds_read_b128 v[64:67], v88 offset:18432
	ds_read_b128 v[60:63], v88 offset:18464
	ds_read_b128 v[56:59], v88 offset:18496
	ds_read_b128 v[52:55], v88 offset:18528
	s_and_b64 vcc, exec, s[22:23]
	s_cbranch_vccz .LBB0_1463
	v_add_u32_e32 v4, s63, v85
	ds_read_b128 v[0:3], v4
	ds_read_b128 v[90:93], v4 offset:32
	ds_read_b128 v[94:97], v4 offset:64
	ds_read_b128 v[98:101], v4 offset:96
	v_add_u32_e32 v74, 0x2000, v84
	s_waitcnt lgkmcnt(3)
	v_mfma_f32_32x32x16_bf16 v[0:15], v[64:67], v[0:3], 0
	s_mov_b64 s[6:7], 0
	s_waitcnt lgkmcnt(2)
	v_mfma_f32_32x32x16_bf16 v[0:15], v[60:63], v[90:93], v[0:15]
	s_waitcnt lgkmcnt(1)
	v_mfma_f32_32x32x16_bf16 v[0:15], v[56:59], v[94:97], v[0:15]
	ds_read2_b64 v[90:93], v74 offset0:128 offset1:130
	ds_read2_b64 v[94:97], v74 offset0:132 offset1:134
	s_waitcnt lgkmcnt(1)
	v_lshlrev_b32_e32 v74, 16, v90
	v_and_b32_e32 v75, 0xffff0000, v90
	v_mfma_f32_32x32x16_bf16 v[0:15], v[52:55], v[98:101], v[0:15]
	s_nop 11
	v_pk_add_f32 v[0:1], v[0:1], v[74:75]
	v_lshlrev_b32_e32 v74, 16, v91
	v_and_b32_e32 v75, 0xffff0000, v91
	v_pk_add_f32 v[2:3], v[2:3], v[74:75]
	v_lshlrev_b32_e32 v74, 16, v92
	v_and_b32_e32 v75, 0xffff0000, v92
	v_pk_add_f32 v[4:5], v[4:5], v[74:75]
	v_lshlrev_b32_e32 v74, 16, v93
	v_and_b32_e32 v75, 0xffff0000, v93
	v_pk_add_f32 v[6:7], v[6:7], v[74:75]
	s_waitcnt lgkmcnt(0)
	v_lshlrev_b32_e32 v74, 16, v94
	v_and_b32_e32 v75, 0xffff0000, v94
	v_pk_add_f32 v[8:9], v[8:9], v[74:75]
	v_lshlrev_b32_e32 v74, 16, v95
	v_and_b32_e32 v75, 0xffff0000, v95
	v_pk_add_f32 v[10:11], v[10:11], v[74:75]
	v_lshlrev_b32_e32 v74, 16, v96
	v_and_b32_e32 v75, 0xffff0000, v96
	v_pk_add_f32 v[12:13], v[12:13], v[74:75]
	v_lshlrev_b32_e32 v74, 16, v97
	v_and_b32_e32 v75, 0xffff0000, v97
	v_pk_add_f32 v[14:15], v[14:15], v[74:75]
